# layer0 LDS-index gather loop hand-rewritten: 2 rotating edge slots in flight, fma_mix f16->f32 adds, SADDR addressing, no store-ack wait per edge
# speedup vs baseline: 1.0120x; 1.0043x over previous
.LBB4_45:
	v_or_b32_e32 v17, 1, v31
	v_add_u32_e32 v14, s30, v17
	v_min_i32_e32 v14, 0x1869f, v14
	v_lshl_add_u32 v14, v14, 8, v26
	global_load_dwordx4 v[10:13], v14, s[24:25]
	s_mov_b64 s[28:29], exec
	s_movk_i32 s0, 0x4400
	v_subrev_u32_e32 v1, s20, v32
	v_lshl_add_u32 v1, v1, 2, s0
	v_lshl_add_u32 v16, v32, 8, v26
	v_cmp_lt_i32_e64 s[2:3], v32, v33
	v_add_u32_e32 v14, 1, v32
	v_cmp_lt_i32_e64 s[8:9], v14, v33
	s_mov_b64 exec, s[2:3]
	ds_read_b32 v18, v1
	ds_read_b32 v19, v1 offset:4096
	s_waitcnt lgkmcnt(0)
	v_lshl_add_u32 v18, v18, 9, v26
	v_lshl_add_u32 v19, v19, 8, v26
	global_load_dwordx4 v[34:37], v18, s[4:5] offset:256 nt
	global_load_dwordx4 v[20:23], v18, s[4:5] nt
	global_load_dwordx4 v[38:41], v19, s[24:25]
	ds_read_b32 v18, v1 offset:8
	ds_read_b32 v19, v1 offset:4104
	s_mov_b64 exec, s[8:9]
	ds_read_b32 v24, v1 offset:4
	ds_read_b32 v25, v1 offset:4100
	s_waitcnt lgkmcnt(0)
	v_lshl_add_u32 v24, v24, 9, v26
	v_lshl_add_u32 v25, v25, 8, v26
	global_load_dwordx4 v[50:53], v24, s[4:5] offset:256 nt
	global_load_dwordx4 v[46:49], v24, s[4:5] nt
	global_load_dwordx4 v[54:57], v25, s[24:25]
	ds_read_b32 v24, v1 offset:12
	ds_read_b32 v25, v1 offset:4108
	s_mov_b64 exec, s[28:29]
	s_cmp_eq_u64 s[2:3], 0
	s_cbranch_scc1 .Ll0_p1_empty
	s_waitcnt vmcnt(3)
	s_branch .Ll0_p1_body
.Ll0_p1_loop:
	s_waitcnt vmcnt(4)
.Ll0_p1_body:
	s_mov_b64 exec, s[2:3]
	v_cvt_pk_f16_f32 v20, v20, v21
	v_cvt_pk_f16_f32 v21, v22, v23
	v_cvt_pk_f16_f32 v22, v34, v35
	v_cvt_pk_f16_f32 v23, v36, v37
	global_store_dwordx4 v16, v[20:23], s[6:7] offset:0 sc1
	v_fma_mix_f32 v14, v38, 1.0, v20 op_sel_hi:[1,0,1]
	v_fma_mix_f32 v15, v38, 1.0, v20 op_sel:[1,0,1] op_sel_hi:[1,0,1]
	v_fma_mix_f32 v58, v39, 1.0, v21 op_sel_hi:[1,0,1]
	v_fma_mix_f32 v59, v39, 1.0, v21 op_sel:[1,0,1] op_sel_hi:[1,0,1]
	v_max_f32_e32 v14, 0, v14
	v_max_f32_e32 v15, 0, v15
	v_max_f32_e32 v58, 0, v58
	v_max_f32_e32 v59, 0, v59
	v_pk_add_f32 v[2:3], v[2:3], v[14:15]
	v_pk_add_f32 v[4:5], v[4:5], v[58:59]
	v_fma_mix_f32 v14, v40, 1.0, v22 op_sel_hi:[1,0,1]
	v_fma_mix_f32 v15, v40, 1.0, v22 op_sel:[1,0,1] op_sel_hi:[1,0,1]
	v_fma_mix_f32 v58, v41, 1.0, v23 op_sel_hi:[1,0,1]
	v_fma_mix_f32 v59, v41, 1.0, v23 op_sel:[1,0,1] op_sel_hi:[1,0,1]
	v_max_f32_e32 v14, 0, v14
	v_max_f32_e32 v15, 0, v15
	v_max_f32_e32 v58, 0, v58
	v_max_f32_e32 v59, 0, v59
	v_pk_add_f32 v[6:7], v[6:7], v[14:15]
	v_pk_add_f32 v[8:9], v[8:9], v[58:59]
	v_add_u32_e32 v14, 2, v32
	v_cmp_lt_i32_e64 s[2:3], v14, v33
	s_mov_b64 exec, s[2:3]
	s_waitcnt lgkmcnt(0)
	v_lshl_add_u32 v18, v18, 9, v26
	v_lshl_add_u32 v19, v19, 8, v26
	global_load_dwordx4 v[34:37], v18, s[4:5] offset:256 nt
	global_load_dwordx4 v[20:23], v18, s[4:5] nt
	global_load_dwordx4 v[38:41], v19, s[24:25]
	ds_read_b32 v18, v1 offset:16
	ds_read_b32 v19, v1 offset:4112
	s_mov_b64 exec, s[8:9]
	s_waitcnt vmcnt(4)
	v_cvt_pk_f16_f32 v46, v46, v47
	v_cvt_pk_f16_f32 v47, v48, v49
	v_cvt_pk_f16_f32 v48, v50, v51
	v_cvt_pk_f16_f32 v49, v52, v53
	global_store_dwordx4 v16, v[46:49], s[6:7] offset:256 sc1
	v_fma_mix_f32 v14, v54, 1.0, v46 op_sel_hi:[1,0,1]
	v_fma_mix_f32 v15, v54, 1.0, v46 op_sel:[1,0,1] op_sel_hi:[1,0,1]
	v_fma_mix_f32 v58, v55, 1.0, v47 op_sel_hi:[1,0,1]
	v_fma_mix_f32 v59, v55, 1.0, v47 op_sel:[1,0,1] op_sel_hi:[1,0,1]
	v_max_f32_e32 v14, 0, v14
	v_max_f32_e32 v15, 0, v15
	v_max_f32_e32 v58, 0, v58
	v_max_f32_e32 v59, 0, v59
	v_pk_add_f32 v[2:3], v[2:3], v[14:15]
	v_pk_add_f32 v[4:5], v[4:5], v[58:59]
	v_fma_mix_f32 v14, v56, 1.0, v48 op_sel_hi:[1,0,1]
	v_fma_mix_f32 v15, v56, 1.0, v48 op_sel:[1,0,1] op_sel_hi:[1,0,1]
	v_fma_mix_f32 v58, v57, 1.0, v49 op_sel_hi:[1,0,1]
	v_fma_mix_f32 v59, v57, 1.0, v49 op_sel:[1,0,1] op_sel_hi:[1,0,1]
	v_max_f32_e32 v14, 0, v14
	v_max_f32_e32 v15, 0, v15
	v_max_f32_e32 v58, 0, v58
	v_max_f32_e32 v59, 0, v59
	v_pk_add_f32 v[6:7], v[6:7], v[14:15]
	v_pk_add_f32 v[8:9], v[8:9], v[58:59]
	v_add_u32_e32 v14, 3, v32
	v_cmp_lt_i32_e64 s[8:9], v14, v33
	s_mov_b64 exec, s[8:9]
	s_waitcnt lgkmcnt(0)
	v_lshl_add_u32 v24, v24, 9, v26
	v_lshl_add_u32 v25, v25, 8, v26
	global_load_dwordx4 v[50:53], v24, s[4:5] offset:256 nt
	global_load_dwordx4 v[46:49], v24, s[4:5] nt
	global_load_dwordx4 v[54:57], v25, s[24:25]
	ds_read_b32 v24, v1 offset:20
	ds_read_b32 v25, v1 offset:4116
	s_mov_b64 exec, s[28:29]
	v_add_u32_e32 v32, 2, v32
	v_add_u32_e32 v1, 8, v1
	v_add_u32_e32 v16, 0x200, v16
	s_cmp_lg_u64 s[2:3], 0
	s_cbranch_scc1 .Ll0_p1_loop
	s_branch .Ll0_p1_done

.Ll0_p1_done:
	s_movk_i32 s2, 0x110
	v_cvt_pk_f16_f32 v21, v8, v9
	v_cvt_pk_f16_f32 v20, v6, v7
	v_cvt_pk_f16_f32 v19, v4, v5
	v_cvt_pk_f16_f32 v18, v2, v3
	v_mad_u32_u24 v14, v44, s2, v26
	ds_write_b128 v14, v[18:21]
	v_mov_b32_e32 v14, 0x6400
	v_lshl_or_b32 v14, v17, 2, v14
	ds_read2_b32 v[32:33], v14 offset1:1
	v_add_u32_e32 v14, s30, v17
	s_mov_b32 s2, 0x186a0
	v_cmp_gt_i32_e32 vcc, s2, v14
	v_cvt_f32_f16_e32 v2, v10
	v_cvt_f32_f16_sdwa v3, v10 dst_sel:DWORD dst_unused:UNUSED_PAD src0_sel:WORD_1
	v_cvt_f32_f16_e32 v4, v11
	v_cvt_f32_f16_sdwa v5, v11 dst_sel:DWORD dst_unused:UNUSED_PAD src0_sel:WORD_1
	v_cvt_f32_f16_e32 v6, v12
	v_cvt_f32_f16_sdwa v7, v12 dst_sel:DWORD dst_unused:UNUSED_PAD src0_sel:WORD_1
	v_cvt_f32_f16_e32 v8, v13
	v_cvt_f32_f16_sdwa v9, v13 dst_sel:DWORD dst_unused:UNUSED_PAD src0_sel:WORD_1
	v_pk_mul_f32 v[2:3], v[30:31], v[2:3] op_sel_hi:[0,1]
	v_pk_mul_f32 v[4:5], v[30:31], v[4:5] op_sel_hi:[0,1]
	v_pk_mul_f32 v[6:7], v[30:31], v[6:7] op_sel_hi:[0,1]
	v_pk_mul_f32 v[8:9], v[30:31], v[8:9] op_sel_hi:[0,1]
	v_cndmask_b32_e32 v2, 0, v2, vcc
	v_cndmask_b32_e32 v3, 0, v3, vcc
	v_cndmask_b32_e32 v4, 0, v4, vcc
	v_cndmask_b32_e32 v5, 0, v5, vcc
	v_cndmask_b32_e32 v6, 0, v6, vcc
	v_cndmask_b32_e32 v7, 0, v7, vcc
	v_cndmask_b32_e32 v8, 0, v8, vcc
	v_cndmask_b32_e32 v9, 0, v9, vcc
	s_waitcnt lgkmcnt(0)
	v_subrev_u32_e32 v1, s20, v32
	v_lshl_add_u32 v1, v1, 2, s0
	v_lshl_add_u32 v16, v32, 8, v26
	v_cmp_lt_i32_e64 s[2:3], v32, v33
	v_add_u32_e32 v14, 1, v32
	v_cmp_lt_i32_e64 s[8:9], v14, v33
	s_mov_b64 exec, s[2:3]
	ds_read_b32 v18, v1
	ds_read_b32 v19, v1 offset:4096
	s_waitcnt lgkmcnt(0)
	v_lshl_add_u32 v18, v18, 9, v26
	v_lshl_add_u32 v19, v19, 8, v26
	global_load_dwordx4 v[34:37], v18, s[4:5] offset:256 nt
	global_load_dwordx4 v[20:23], v18, s[4:5] nt
	global_load_dwordx4 v[38:41], v19, s[24:25]
	ds_read_b32 v18, v1 offset:8
	ds_read_b32 v19, v1 offset:4104
	s_mov_b64 exec, s[8:9]
	ds_read_b32 v24, v1 offset:4
	ds_read_b32 v25, v1 offset:4100
	s_waitcnt lgkmcnt(0)
	v_lshl_add_u32 v24, v24, 9, v26
	v_lshl_add_u32 v25, v25, 8, v26
	global_load_dwordx4 v[50:53], v24, s[4:5] offset:256 nt
	global_load_dwordx4 v[46:49], v24, s[4:5] nt
	global_load_dwordx4 v[54:57], v25, s[24:25]
	ds_read_b32 v24, v1 offset:12
	ds_read_b32 v25, v1 offset:4108
	s_mov_b64 exec, s[28:29]
	s_cmp_eq_u64 s[2:3], 0
	s_cbranch_scc1 .Ll0_p2_empty
	s_waitcnt vmcnt(3)
	s_branch .Ll0_p2_body

.Ll0_p2_done:
	v_mov_b32_e32 v1, v17
	v_mov_b64_e32 v[16:17], v[8:9]
	v_mov_b64_e32 v[14:15], v[6:7]
	v_mov_b64_e32 v[12:13], v[4:5]
	v_mov_b64_e32 v[10:11], v[2:3]
	s_branch .LBB4_70

.LBB4_54:
	s_or_b64 exec, exec, s[2:3]
	s_waitcnt lgkmcnt(0)
	v_cmp_lt_i32_e64 s[0:1], v32, v33
	v_mov_b64_e32 v[16:17], v[8:9]
	v_mov_b64_e32 v[14:15], v[6:7]
	v_mov_b64_e32 v[12:13], v[4:5]
	v_mov_b64_e32 v[10:11], v[2:3]
	s_and_saveexec_b64 s[2:3], s[0:1]
	s_cbranch_execz .LBB4_62
	v_ashrrev_i32_e32 v11, 31, v32
	v_mov_b32_e32 v10, v32
	v_lshlrev_b64 v[12:13], 8, v[10:11]
	v_lshlrev_b64 v[10:11], 2, v[10:11]
	v_lshl_add_u64 v[34:35], s[10:11], 0, v[10:11]
	v_lshl_add_u64 v[36:37], s[22:23], 0, v[10:11]
	v_add_u32_e32 v10, 1, v32
	v_ashrrev_i32_e32 v11, 31, v10
	v_lshlrev_b64 v[10:11], 8, v[10:11]
	v_lshl_add_u64 v[30:31], v[28:29], 0, v[12:13]
	v_lshl_add_u64 v[38:39], v[28:29], 0, v[10:11]
	v_mov_b64_e32 v[16:17], v[8:9]
	s_mov_b64 s[0:1], 0
	s_mov_b64 s[4:5], 0x200
	v_mov_b64_e32 v[14:15], v[6:7]
	v_mov_b64_e32 v[12:13], v[4:5]
	v_mov_b64_e32 v[10:11], v[2:3]
	v_mov_b32_e32 v27, v32
	s_branch .LBB4_58

.LBB4_58:
	global_load_dword v18, v[36:37], off
	global_load_dword v20, v[34:35], off
	v_add_u32_e32 v40, 1, v27
	v_cmp_lt_i32_e32 vcc, v40, v33
	s_waitcnt vmcnt(1)
	v_ashrrev_i32_e32 v19, 31, v18
	v_lshlrev_b64 v[18:19], 9, v[18:19]
	v_lshl_add_u64 v[18:19], v[24:25], 0, v[18:19]
	global_load_dwordx4 v[44:47], v[18:19], off offset:256 nt
	global_load_dwordx4 v[48:51], v[18:19], off nt
	s_waitcnt vmcnt(2)
	v_ashrrev_i32_e32 v21, 31, v20
	v_lshlrev_b64 v[18:19], 8, v[20:21]
	v_lshl_add_u64 v[18:19], v[22:23], 0, v[18:19]
	global_load_dwordx4 v[18:21], v[18:19], off
	s_waitcnt vmcnt(2)
	v_cvt_f16_f32_e32 v41, v47
	v_cvt_f16_f32_e32 v52, v46
	v_cvt_f16_f32_e32 v53, v45
	v_cvt_f16_f32_e32 v54, v44
	s_waitcnt vmcnt(1)
	v_cvt_f16_f32_e32 v55, v51
	v_cvt_f16_f32_e32 v56, v50
	v_cvt_f16_f32_e32 v57, v49
	v_cvt_f16_f32_e32 v58, v48
	v_cvt_pk_f16_f32 v47, v46, v47
	v_cvt_pk_f16_f32 v46, v44, v45
	v_cvt_pk_f16_f32 v45, v50, v51
	v_cvt_pk_f16_f32 v44, v48, v49
	s_waitcnt vmcnt(0)
	v_cvt_f32_f16_e32 v48, v18
	v_cvt_f32_f16_sdwa v18, v18 dst_sel:DWORD dst_unused:UNUSED_PAD src0_sel:WORD_1
	v_cvt_f32_f16_e32 v49, v19
	v_cvt_f32_f16_sdwa v19, v19 dst_sel:DWORD dst_unused:UNUSED_PAD src0_sel:WORD_1
	v_cvt_f32_f16_e32 v50, v20
	v_cvt_f32_f16_sdwa v20, v20 dst_sel:DWORD dst_unused:UNUSED_PAD src0_sel:WORD_1
	v_cvt_f32_f16_e32 v51, v21
	v_cvt_f32_f16_sdwa v21, v21 dst_sel:DWORD dst_unused:UNUSED_PAD src0_sel:WORD_1
	global_store_dwordx4 v[30:31], v[44:47], off sc1
	s_nop 1
	v_cvt_f32_f16_e32 v44, v58
	v_cvt_f32_f16_e32 v45, v57
	v_cvt_f32_f16_e32 v46, v56
	v_cvt_f32_f16_e32 v47, v55
	v_cvt_f32_f16_e32 v54, v54
	v_cvt_f32_f16_e32 v53, v53
	v_cvt_f32_f16_e32 v52, v52
	v_cvt_f32_f16_e32 v41, v41
	v_add_f32_e32 v44, v44, v48
	v_add_f32_e32 v45, v18, v45
	v_add_f32_e32 v46, v49, v46
	v_add_f32_e32 v47, v19, v47
	v_add_f32_e32 v48, v50, v54
	v_add_f32_e32 v49, v20, v53
	v_add_f32_e32 v50, v51, v52
	v_add_f32_e32 v41, v21, v41
	v_max_f32_e32 v18, 0, v44
	v_max_f32_e32 v19, 0, v45
	v_max_f32_e32 v20, 0, v46
	v_max_f32_e32 v21, 0, v47
	v_max_f32_e32 v44, 0, v48
	v_max_f32_e32 v45, 0, v49
	v_max_f32_e32 v46, 0, v50
	v_max_f32_e32 v47, 0, v41
	v_pk_add_f32 v[10:11], v[10:11], v[18:19]
	v_pk_add_f32 v[12:13], v[12:13], v[20:21]
	v_pk_add_f32 v[14:15], v[14:15], v[44:45]
	v_pk_add_f32 v[16:17], v[16:17], v[46:47]
	s_and_saveexec_b64 s[6:7], vcc
	s_cbranch_execz .LBB4_57
	v_cndmask_b32_e32 v18, v27, v40, vcc
	v_ashrrev_i32_e32 v19, 31, v18
	v_lshlrev_b64 v[18:19], 2, v[18:19]
	v_lshl_add_u64 v[20:21], s[22:23], 0, v[18:19]
	global_load_dword v20, v[20:21], off
	v_lshl_add_u64 v[18:19], s[10:11], 0, v[18:19]
	global_load_dword v40, v[18:19], off
	s_waitcnt vmcnt(1)
	v_ashrrev_i32_e32 v21, 31, v20
	v_lshlrev_b64 v[18:19], 9, v[20:21]
	v_lshl_add_u64 v[44:45], v[24:25], 0, v[18:19]
	global_load_dwordx4 v[18:21], v[44:45], off offset:256 nt
	s_nop 0
	global_load_dwordx4 v[44:47], v[44:45], off nt
	s_waitcnt vmcnt(2)
	v_ashrrev_i32_e32 v41, 31, v40
	v_lshlrev_b64 v[40:41], 8, v[40:41]
	v_lshl_add_u64 v[40:41], v[22:23], 0, v[40:41]
	global_load_dwordx4 v[48:51], v[40:41], off
	s_waitcnt vmcnt(2)
	v_cvt_f16_f32_e32 v40, v21
	v_cvt_f16_f32_e32 v41, v20
	v_cvt_f16_f32_e32 v52, v19
	v_cvt_f16_f32_e32 v53, v18
	s_waitcnt vmcnt(1)
	v_cvt_f16_f32_e32 v54, v47
	v_cvt_f16_f32_e32 v55, v46
	v_cvt_f16_f32_e32 v56, v45
	v_cvt_f16_f32_e32 v57, v44
	v_cvt_pk_f16_f32 v21, v20, v21
	v_cvt_pk_f16_f32 v20, v18, v19
	v_cvt_pk_f16_f32 v19, v46, v47
	v_cvt_pk_f16_f32 v18, v44, v45
	s_waitcnt vmcnt(0)
	v_cvt_f32_f16_e32 v44, v48
	v_cvt_f32_f16_sdwa v45, v48 dst_sel:DWORD dst_unused:UNUSED_PAD src0_sel:WORD_1
	v_cvt_f32_f16_e32 v46, v49
	v_cvt_f32_f16_sdwa v47, v49 dst_sel:DWORD dst_unused:UNUSED_PAD src0_sel:WORD_1
	v_cvt_f32_f16_e32 v48, v50
	v_cvt_f32_f16_sdwa v49, v50 dst_sel:DWORD dst_unused:UNUSED_PAD src0_sel:WORD_1
	v_cvt_f32_f16_e32 v50, v51
	v_cvt_f32_f16_sdwa v51, v51 dst_sel:DWORD dst_unused:UNUSED_PAD src0_sel:WORD_1
	global_store_dwordx4 v[38:39], v[18:21], off sc1
	s_nop 1
	v_cvt_f32_f16_e32 v18, v57
	v_cvt_f32_f16_e32 v19, v56
	v_cvt_f32_f16_e32 v20, v55
	v_cvt_f32_f16_e32 v21, v54
	v_cvt_f32_f16_e32 v53, v53
	v_cvt_f32_f16_e32 v52, v52
	v_cvt_f32_f16_e32 v41, v41
	v_cvt_f32_f16_e32 v40, v40
	v_add_f32_e32 v18, v44, v18
	v_add_f32_e32 v19, v45, v19
	v_add_f32_e32 v20, v46, v20
	v_add_f32_e32 v21, v47, v21
	v_add_f32_e32 v44, v48, v53
	v_add_f32_e32 v45, v49, v52
	v_add_f32_e32 v46, v50, v41
	v_add_f32_e32 v47, v51, v40
	v_max_f32_e32 v18, 0, v18
	v_max_f32_e32 v19, 0, v19
	v_max_f32_e32 v20, 0, v20
	v_max_f32_e32 v21, 0, v21
	v_max_f32_e32 v40, 0, v44
	v_max_f32_e32 v41, 0, v45
	v_max_f32_e32 v44, 0, v46
	v_max_f32_e32 v45, 0, v47
	v_pk_add_f32 v[10:11], v[18:19], v[10:11]
	v_pk_add_f32 v[12:13], v[20:21], v[12:13]
	v_pk_add_f32 v[14:15], v[40:41], v[14:15]
	v_pk_add_f32 v[16:17], v[44:45], v[16:17]
	s_branch .LBB4_57
.LBB4_61:
	s_or_b64 exec, exec, s[0:1]
.LBB4_62:
	s_or_b64 exec, exec, s[2:3]
.LBB4_70:
	v_lshlrev_b32_e32 v2, 4, v0
	global_load_dwordx4 v[6:9], v2, s[18:19]
	v_mov_b32_e32 v3, 0
	v_lshl_add_u64 v[22:23], s[18:19], 0, v[2:3]
	v_add_co_u32_e32 v2, vcc, 0x2000, v22
	v_cvt_pk_f16_f32 v17, v16, v17
	s_nop 0
	v_addc_co_u32_e32 v3, vcc, 0, v23, vcc
	s_waitcnt lgkmcnt(0)
	global_load_dwordx4 v[18:21], v[2:3], off
	v_add_co_u32_e32 v2, vcc, 0x4000, v22
	v_cvt_pk_f16_f32 v16, v14, v15
	s_nop 0
	v_addc_co_u32_e32 v3, vcc, 0, v23, vcc
	global_load_dwordx4 v[2:5], v[2:3], off
	v_cvt_pk_f16_f32 v14, v10, v11
	s_movk_i32 s2, 0x110
	v_add_co_u32_e32 v10, vcc, 0x6000, v22
	v_cvt_pk_f16_f32 v15, v12, v13
	v_mad_u32_u24 v1, v1, s2, v26
	v_addc_co_u32_e32 v11, vcc, 0, v23, vcc
	ds_write_b128 v1, v[14:17]
	global_load_dwordx4 v[14:17], v[10:11], off
	v_and_b32_e32 v27, 48, v0
	v_mad_u32_u24 v40, v42, s2, v27
	s_waitcnt lgkmcnt(0)
	s_barrier
	ds_read_b128 v[10:13], v40
	ds_read_b128 v[22:25], v40 offset:64
	ds_read_b128 v[28:31], v40 offset:4352
	ds_read_b128 v[32:35], v40 offset:4416
	ds_read_b128 v[36:39], v40 offset:8704
	ds_read_b128 v[44:47], v40 offset:8768
	ds_read_b128 v[48:51], v40 offset:13056
	ds_read_b128 v[52:55], v40 offset:13120
	v_mbcnt_hi_u32_b32 v1, -1, v43
	s_waitcnt vmcnt(3) lgkmcnt(7)
	v_mfma_f32_16x16x32_f16 v[10:13], v[10:13], v[6:9], 0
	s_waitcnt lgkmcnt(5)
	v_mfma_f32_16x16x32_f16 v[28:31], v[28:31], v[6:9], 0
	s_waitcnt lgkmcnt(3)
	v_mfma_f32_16x16x32_f16 v[36:39], v[36:39], v[6:9], 0
	s_waitcnt lgkmcnt(1)
	v_mfma_f32_16x16x32_f16 v[6:9], v[48:51], v[6:9], 0
	s_waitcnt vmcnt(2)
	v_mfma_f32_16x16x32_f16 v[10:13], v[22:25], v[18:21], v[10:13]
	v_mfma_f32_16x16x32_f16 v[22:25], v[32:35], v[18:21], v[28:31]
	v_mfma_f32_16x16x32_f16 v[28:31], v[44:47], v[18:21], v[36:39]
	s_waitcnt lgkmcnt(0)
	v_mfma_f32_16x16x32_f16 v[6:9], v[52:55], v[18:21], v[6:9]
	ds_read_b128 v[18:21], v40 offset:128
	ds_read_b128 v[32:35], v40 offset:192
	s_waitcnt vmcnt(1) lgkmcnt(1)
	v_mfma_f32_16x16x32_f16 v[10:13], v[18:21], v[2:5], v[10:13]
	ds_read_b128 v[18:21], v40 offset:4480
	ds_read_b128 v[36:39], v40 offset:4544
	s_waitcnt lgkmcnt(1)
	v_mfma_f32_16x16x32_f16 v[44:47], v[18:21], v[2:5], v[22:25]
	ds_read_b128 v[18:21], v40 offset:8832
	ds_read_b128 v[48:51], v40 offset:8896
	s_waitcnt lgkmcnt(1)
	v_mfma_f32_16x16x32_f16 v[28:31], v[18:21], v[2:5], v[28:31]
	ds_read_b128 v[22:25], v40 offset:13184
	ds_read_b128 v[18:21], v40 offset:13248
	s_waitcnt lgkmcnt(1)
	v_mfma_f32_16x16x32_f16 v[22:25], v[22:25], v[2:5], v[6:9]
	v_and_b32_e32 v2, 64, v1
	s_waitcnt vmcnt(0)
	v_mfma_f32_16x16x32_f16 v[10:13], v[32:35], v[14:17], v[10:13]
	v_add_u32_e32 v34, 64, v2
	v_xor_b32_e32 v32, 16, v1
	v_cmp_lt_i32_e32 vcc, v32, v34
	v_mfma_f32_16x16x32_f16 v[6:9], v[36:39], v[14:17], v[44:47]
	v_xor_b32_e32 v33, 32, v1
	v_mfma_f32_16x16x32_f16 v[2:5], v[48:51], v[14:17], v[28:31]
	s_waitcnt lgkmcnt(0)
	v_mfma_f32_16x16x32_f16 v[14:17], v[18:21], v[14:17], v[22:25]
	v_add_f32_e32 v18, 0, v10
	v_mul_f32_e32 v19, v11, v11
	v_add_f32_e32 v18, v18, v11
	v_fmac_f32_e32 v19, v10, v10
	v_add_f32_e32 v18, v18, v12
	v_fmac_f32_e32 v19, v12, v12
	v_add_f32_e32 v18, v18, v13
	v_fmac_f32_e32 v19, v13, v13
	v_add_f32_e32 v18, v18, v6
	v_fmac_f32_e32 v19, v6, v6
	v_add_f32_e32 v18, v18, v7
	v_fmac_f32_e32 v19, v7, v7
	v_add_f32_e32 v18, v18, v8
	v_fmac_f32_e32 v19, v8, v8
	v_add_f32_e32 v18, v18, v9
	v_fmac_f32_e32 v19, v9, v9
	v_add_f32_e32 v18, v18, v2
	v_fmac_f32_e32 v19, v2, v2
	v_add_f32_e32 v18, v18, v3
	v_fmac_f32_e32 v19, v3, v3
	v_add_f32_e32 v18, v18, v4
	v_fmac_f32_e32 v19, v4, v4
	v_add_f32_e32 v18, v18, v5
	v_fmac_f32_e32 v19, v5, v5
	v_add_f32_e32 v18, v18, v14
	v_fmac_f32_e32 v19, v14, v14
	v_add_f32_e32 v18, v18, v15
	v_fmac_f32_e32 v19, v15, v15
	v_cndmask_b32_e32 v28, v1, v32, vcc
	v_add_f32_e32 v18, v18, v16
	v_fmac_f32_e32 v19, v16, v16
	v_lshlrev_b32_e32 v28, 2, v28
	v_add_f32_e32 v18, v18, v17
	v_fmac_f32_e32 v19, v17, v17
	ds_bpermute_b32 v20, v28, v18
	ds_bpermute_b32 v21, v28, v19
	v_cmp_lt_i32_e32 vcc, v33, v34
	s_waitcnt lgkmcnt(1)
	v_add_f32_e32 v18, v18, v20
	v_cndmask_b32_e32 v1, v1, v33, vcc
	v_lshlrev_b32_e32 v1, 2, v1
	s_waitcnt lgkmcnt(0)
	v_add_f32_e32 v19, v19, v21
	ds_bpermute_b32 v20, v1, v18
	ds_bpermute_b32 v21, v1, v19
	v_lshrrev_b32_e32 v1, 6, v0
	v_cmp_eq_u32_e32 vcc, 0, v27
	s_and_saveexec_b64 s[0:1], vcc
	s_cbranch_execz .LBB4_72
	s_lshr_b32 s3, s15, 29
	s_add_i32 s3, s14, s3
	s_and_b32 s3, s3, 0xfffff8
	s_sub_i32 s3, s14, s3
	s_lshl_b32 s4, s3, 8
	s_ashr_i32 s5, s4, 31
	s_lshl_b64 s[4:5], s[4:5], 2
	s_add_u32 s4, s16, s4
	v_lshlrev_b32_e32 v22, 2, v42
	s_addc_u32 s5, s17, s5
	v_lshl_or_b32 v22, v1, 6, v22
	s_waitcnt lgkmcnt(1)
	v_add_f32_e32 v18, v18, v20
	s_waitcnt lgkmcnt(0)
	v_add_f32_e32 v19, v19, v21
	global_atomic_add_f32 v22, v18, s[4:5]
	global_atomic_add_f32 v22, v19, s[4:5] offset:512
